# baseline (speedup 1.0000x reference)
.LBB5_93:
	s_mul_hi_i32 s7, s37, 0x300
	s_mul_i32 s6, s37, 0x300
	s_lshl_b64 s[14:15], s[6:7], 2
	s_add_u32 s6, s28, s14
	s_addc_u32 s7, s29, s15
	s_add_u32 s8, s30, s14
	s_addc_u32 s9, s31, s15
	v_add_f32_dpp v1, v71, v71 quad_perm:[1,0,3,2] row_mask:0xf bank_mask:0xf bound_ctrl:1
	v_cmp_eq_u32_e64 s[6:7], 0, v128
	s_nop 0
	v_add_f32_dpp v1, v1, v1 quad_perm:[2,3,0,1] row_mask:0xf bank_mask:0xf bound_ctrl:1
	s_nop 1
	v_add_f32_dpp v1, v1, v1 row_half_mirror row_mask:0xf bank_mask:0xf bound_ctrl:1
	s_nop 1
	v_add_f32_dpp v1, v1, v1 row_mirror row_mask:0xf bank_mask:0xf bound_ctrl:1
	s_nop 0
	v_readlane_b32 s8, v1, 0
	v_readlane_b32 s29, v1, 16
	v_readlane_b32 s16, v1, 32
	v_readlane_b32 s28, v1, 48
	v_add_f32_dpp v1, v70, v70 quad_perm:[1,0,3,2] row_mask:0xf bank_mask:0xf bound_ctrl:1
	s_nop 1
	v_add_f32_dpp v1, v1, v1 quad_perm:[2,3,0,1] row_mask:0xf bank_mask:0xf bound_ctrl:1
	s_nop 1
	v_add_f32_dpp v1, v1, v1 row_half_mirror row_mask:0xf bank_mask:0xf bound_ctrl:1
	s_nop 1
	v_add_f32_dpp v1, v1, v1 row_mirror row_mask:0xf bank_mask:0xf bound_ctrl:1
	s_nop 0
	v_readlane_b32 s9, v1, 0
	v_readlane_b32 s31, v1, 16
	v_readlane_b32 s17, v1, 32
	v_readlane_b32 s30, v1, 48
	s_and_saveexec_b64 s[18:19], s[6:7]
	s_xor_b64 s[18:19], exec, s[18:19]
	s_cbranch_execz .LBB5_99
	s_lshl_b32 s37, s45, 3
	v_mov_b32_e32 v42, s29
	v_mov_b32_e32 v43, s31
	v_mov_b32_e32 v44, s28
	v_mov_b32_e32 v45, s30
	s_add_i32 s37, s37, 0x23e40
	v_pk_add_f32 v[42:43], s[8:9], v[42:43]
	v_pk_add_f32 v[44:45], s[16:17], v[44:45]
	v_mov_b32_e32 v1, s37
	v_pk_add_f32 v[42:43], v[42:43], v[44:45]
	ds_write_b64 v1, v[42:43]

.LBB5_101:
	s_or_b64 exec, exec, s[16:17]
	s_movk_i32 s58, 0x3000
	v_add_co_u32_e32 v26, vcc, s58, v84
	v_or_b32_e32 v1, 0x800, v0
	s_nop 0
	v_addc_co_u32_e32 v27, vcc, 0, v85, vcc
	v_add_co_u32_e32 v28, vcc, 0x5000, v84
	s_movk_i32 s58, 0xb00
	s_nop 0
	v_addc_co_u32_e32 v29, vcc, 0, v85, vcc
	global_load_dwordx4 v[30:33], v[26:27], off
	global_load_dwordx4 v[34:37], v[28:29], off offset:2048
	v_cmp_gt_u32_e64 s[12:13], s58, v1
	s_and_saveexec_b64 s[56:57], s[12:13]
	s_cbranch_execz .LBB5_95
	v_lshlrev_b32_e32 v1, 4, v1
	global_load_dwordx4 v[26:29], v1, s[42:43]
.LBB5_95:
	s_or_b64 exec, exec, s[56:57]
	s_and_saveexec_b64 s[56:57], s[10:11]
	s_cbranch_execz .LBB5_97
	v_add_co_u32_e32 v38, vcc, 0xa000, v84
	s_nop 1
	v_addc_co_u32_e32 v39, vcc, 0, v85, vcc
	global_load_dwordx4 v[38:41], v[38:39], off offset:2048
.LBB5_97:
	s_or_b64 exec, exec, s[56:57]
	s_waitcnt vmcnt(1)
	ds_write_b128 v78, v[30:33] offset:12288
	s_waitcnt vmcnt(0)
	ds_write_b128 v78, v[34:37] offset:22528
	s_and_saveexec_b64 s[16:17], s[12:13]
	s_cbranch_execz .LBB5_103
	ds_write_b128 v78, v[26:29] offset:32768
	s_or_b64 exec, exec, s[16:17]
	s_and_saveexec_b64 s[12:13], s[10:11]
	s_branch .LBB5_104
